# v100 + P5 deferred store issued after the first interval's counted wait instead of at the loop top (one more interval before its acknowledgement is needed)
# speedup vs baseline: 1.0014x; 1.0014x over previous
.LBB0_869:
	s_mov_b32 s98, 0
	s_cmp_lt_u32 s65, 16
	s_cselect_b64 s[10:11], -1, 0
	s_and_b64 s[10:11], s[24:25], s[10:11]
	s_andn2_b64 vcc, exec, s[10:11]
	s_cbranch_vccnz .LBB0_907
	s_cmp_lt_i32 s65, 6
	s_cbranch_scc1 .LBB0_876
	s_cmp_gt_i32 s65, 9
	s_cbranch_scc0 .LBB0_877
	s_cmp_gt_i32 s65, 11
	s_cbranch_scc0 .LBB0_878
	s_cmp_eq_u32 s65, 12
	s_mov_b64 s[10:11], -1
	s_cbranch_scc0 .LBB0_875
	s_mov_b64 s[10:11], 0

.LBB0_906:
	v_lshl_add_u64 v[246:247], v[172:173], 0, s[26:27]
	v_mov_b64_e32 v[242:243], v[162:163]
	v_mov_b64_e32 v[244:245], v[164:165]
	s_mov_b32 s98, 1
.LBB0_907:
	v_add_u32_e32 v166, 0x10000, v179
	ds_read_b128 v[162:165], v166
	ds_read_b128 v[182:185], v166 offset:1024
	ds_read_b128 v[186:189], v166 offset:2048
	ds_read_b128 v[190:193], v166 offset:3072
	v_add_u32_e32 v166, 0x14000, v179
	ds_read_b128 v[194:197], v166
	ds_read_b128 v[198:201], v166 offset:1024
	ds_read_b128 v[202:205], v166 offset:2048
	ds_read_b128 v[206:209], v166 offset:3072
	s_add_i32 s10, s45, s64
	s_add_i32 s26, s40, s64
	s_add_i32 s11, s10, 0x1000
	s_addk_i32 s26, 0x1000
	s_cmp_eq_u32 s64, 0
	s_cselect_b32 s29, s62, s11
	s_cselect_b32 s27, s63, s26
	s_add_i32 s26, s29, 0x80
	s_add_i32 s28, s27, 0x80
	s_add_i32 s10, s10, 0x80f80
	s_mov_b32 m0, s55
	ds_read_b128 v[210:213], v180
	ds_read_b128 v[214:217], v180 offset:1024
	ds_read_b128 v[218:221], v180 offset:2048
	ds_read_b128 v[222:225], v180 offset:3072
	ds_read_b128 v[226:229], v180 offset:4096
	ds_read_b128 v[230:233], v180 offset:5120
	ds_read_b128 v[234:237], v180 offset:6144
	ds_read_b128 v[238:241], v180 offset:7168
	buffer_load_dwordx4 v1, s[4:7], s10 offen lds
	s_mov_b32 m0, s56
	s_nop 0
	buffer_load_dwordx4 v175, s[4:7], s10 offen lds
	s_waitcnt vmcnt(8)
	s_waitcnt lgkmcnt(0)
	s_barrier
	s_cmp_eq_u32 s98, 0
	s_cbranch_scc1 .Lp5_nost
	global_store_dwordx4 v[246:247], v[242:245], off
.Lp5_nost:
	s_waitcnt lgkmcnt(7)
	v_mfma_f32_16x16x32_bf16 v[126:129], v[162:165], v[210:213], v[126:129]
	v_mfma_f32_16x16x32_bf16 v[126:129], v[182:185], v[214:217], v[126:129]
	s_waitcnt lgkmcnt(5)
	v_mfma_f32_16x16x32_bf16 v[122:125], v[190:193], v[214:217], v[122:125]
	v_mfma_f32_16x16x32_bf16 v[122:125], v[186:189], v[210:213], v[122:125]
	s_waitcnt lgkmcnt(3)
	v_mfma_f32_16x16x32_bf16 v[114:117], v[186:189], v[218:221], v[114:117]
	v_mfma_f32_16x16x32_bf16 v[114:117], v[190:193], v[222:225], v[114:117]
	s_waitcnt lgkmcnt(1)
	v_mfma_f32_16x16x32_bf16 v[118:121], v[182:185], v[222:225], v[118:121]
	v_mfma_f32_16x16x32_bf16 v[118:121], v[162:165], v[218:221], v[118:121]
	v_mfma_f32_16x16x32_bf16 v[110:113], v[162:165], v[226:229], v[110:113]
	v_mfma_f32_16x16x32_bf16 v[110:113], v[182:185], v[230:233], v[110:113]
	v_mfma_f32_16x16x32_bf16 v[106:109], v[190:193], v[230:233], v[106:109]
	v_mfma_f32_16x16x32_bf16 v[106:109], v[186:189], v[226:229], v[106:109]
	v_mfma_f32_16x16x32_bf16 v[98:101], v[186:189], v[234:237], v[98:101]
	v_mfma_f32_16x16x32_bf16 v[98:101], v[190:193], v[238:241], v[98:101]
	s_waitcnt lgkmcnt(0)
	v_mfma_f32_16x16x32_bf16 v[102:105], v[182:185], v[238:241], v[102:105]
	v_mfma_f32_16x16x32_bf16 v[102:105], v[162:165], v[234:237], v[102:105]
	v_mfma_f32_16x16x32_bf16 v[94:97], v[194:197], v[210:213], v[94:97]
	v_mfma_f32_16x16x32_bf16 v[94:97], v[198:201], v[214:217], v[94:97]
	v_mfma_f32_16x16x32_bf16 v[90:93], v[206:209], v[214:217], v[90:93]
	v_mfma_f32_16x16x32_bf16 v[90:93], v[202:205], v[210:213], v[90:93]
	v_mfma_f32_16x16x32_bf16 v[82:85], v[202:205], v[218:221], v[82:85]
	v_mfma_f32_16x16x32_bf16 v[82:85], v[206:209], v[222:225], v[82:85]
	v_mfma_f32_16x16x32_bf16 v[86:89], v[198:201], v[222:225], v[86:89]
	v_mfma_f32_16x16x32_bf16 v[86:89], v[194:197], v[218:221], v[86:89]
	v_mfma_f32_16x16x32_bf16 v[78:81], v[194:197], v[226:229], v[78:81]
	v_mfma_f32_16x16x32_bf16 v[78:81], v[198:201], v[230:233], v[78:81]
	v_mfma_f32_16x16x32_bf16 v[74:77], v[206:209], v[230:233], v[74:77]
	v_mfma_f32_16x16x32_bf16 v[74:77], v[202:205], v[226:229], v[74:77]
	v_mfma_f32_16x16x32_bf16 v[66:69], v[202:205], v[234:237], v[66:69]
	v_mfma_f32_16x16x32_bf16 v[66:69], v[206:209], v[238:241], v[66:69]
	v_mfma_f32_16x16x32_bf16 v[70:73], v[198:201], v[238:241], v[70:73]
	v_mfma_f32_16x16x32_bf16 v[70:73], v[194:197], v[234:237], v[70:73]
	s_barrier
	s_mov_b32 m0, s37
	s_mov_b32 s10, s6
	s_mov_b32 s11, s7
	ds_read_b128 v[210:213], v180 offset:16384
	ds_read_b128 v[214:217], v180 offset:17408
	ds_read_b128 v[218:221], v180 offset:18432
	ds_read_b128 v[222:225], v180 offset:19456
	ds_read_b128 v[226:229], v180 offset:20480
	ds_read_b128 v[230:233], v180 offset:21504
	ds_read_b128 v[234:237], v180 offset:22528
	ds_read_b128 v[238:241], v180 offset:23552
	buffer_load_dwordx4 v174, s[8:11], s27 offen lds
	s_mov_b32 m0, s38
	s_add_i32 s66, s27, 0x80000
	buffer_load_dwordx4 v176, s[8:11], s27 offen lds
	s_mov_b32 m0, s39
	s_nop 0
	buffer_load_dwordx4 v174, s[8:11], s66 offen lds
	s_mov_b32 m0, s41
	s_nop 0
	buffer_load_dwordx4 v176, s[8:11], s66 offen lds
	s_mov_b32 m0, s36
	s_nop 0
	buffer_load_dwordx4 v1, s[4:7], s29 offen lds
	s_mov_b32 m0, s42
	s_nop 0
	buffer_load_dwordx4 v175, s[4:7], s29 offen lds
	s_waitcnt vmcnt(8)
	s_waitcnt lgkmcnt(0)
	s_barrier
	s_waitcnt lgkmcnt(7)
	v_mfma_f32_16x16x32_bf16 v[62:65], v[162:165], v[210:213], v[62:65]
	v_mfma_f32_16x16x32_bf16 v[62:65], v[182:185], v[214:217], v[62:65]
	s_waitcnt lgkmcnt(5)
	v_mfma_f32_16x16x32_bf16 v[58:61], v[190:193], v[214:217], v[58:61]
	v_mfma_f32_16x16x32_bf16 v[58:61], v[186:189], v[210:213], v[58:61]
	s_waitcnt lgkmcnt(3)
	v_mfma_f32_16x16x32_bf16 v[50:53], v[186:189], v[218:221], v[50:53]
	v_mfma_f32_16x16x32_bf16 v[50:53], v[190:193], v[222:225], v[50:53]
	s_waitcnt lgkmcnt(1)
	v_mfma_f32_16x16x32_bf16 v[54:57], v[182:185], v[222:225], v[54:57]
	v_mfma_f32_16x16x32_bf16 v[54:57], v[162:165], v[218:221], v[54:57]
	v_mfma_f32_16x16x32_bf16 v[46:49], v[162:165], v[226:229], v[46:49]
	v_mfma_f32_16x16x32_bf16 v[46:49], v[182:185], v[230:233], v[46:49]
	v_mfma_f32_16x16x32_bf16 v[42:45], v[190:193], v[230:233], v[42:45]
	v_mfma_f32_16x16x32_bf16 v[42:45], v[186:189], v[226:229], v[42:45]
	v_mfma_f32_16x16x32_bf16 v[34:37], v[186:189], v[234:237], v[34:37]
	v_mfma_f32_16x16x32_bf16 v[34:37], v[190:193], v[238:241], v[34:37]
	s_waitcnt lgkmcnt(0)
	v_mfma_f32_16x16x32_bf16 v[38:41], v[182:185], v[238:241], v[38:41]
	v_mfma_f32_16x16x32_bf16 v[38:41], v[162:165], v[234:237], v[38:41]
	v_mfma_f32_16x16x32_bf16 v[30:33], v[194:197], v[210:213], v[30:33]
	v_mfma_f32_16x16x32_bf16 v[30:33], v[198:201], v[214:217], v[30:33]
	v_mfma_f32_16x16x32_bf16 v[26:29], v[206:209], v[214:217], v[26:29]
	v_mfma_f32_16x16x32_bf16 v[26:29], v[202:205], v[210:213], v[26:29]
	v_mfma_f32_16x16x32_bf16 v[18:21], v[202:205], v[218:221], v[18:21]
	v_mfma_f32_16x16x32_bf16 v[18:21], v[206:209], v[222:225], v[18:21]
	v_mfma_f32_16x16x32_bf16 v[22:25], v[198:201], v[222:225], v[22:25]
	v_mfma_f32_16x16x32_bf16 v[22:25], v[194:197], v[218:221], v[22:25]
	v_mfma_f32_16x16x32_bf16 v[14:17], v[194:197], v[226:229], v[14:17]
	v_mfma_f32_16x16x32_bf16 v[14:17], v[198:201], v[230:233], v[14:17]
	v_mfma_f32_16x16x32_bf16 v[10:13], v[206:209], v[230:233], v[10:13]
	v_mfma_f32_16x16x32_bf16 v[10:13], v[202:205], v[226:229], v[10:13]
	v_mfma_f32_16x16x32_bf16 v[2:5], v[202:205], v[234:237], v[2:5]
	v_mfma_f32_16x16x32_bf16 v[2:5], v[206:209], v[238:241], v[2:5]
	v_mfma_f32_16x16x32_bf16 v[6:9], v[198:201], v[238:241], v[6:9]
	v_mfma_f32_16x16x32_bf16 v[6:9], v[194:197], v[234:237], v[6:9]
	s_barrier
	v_add_u32_e32 v166, 0x18000, v179
	ds_read_b128 v[162:165], v166
	ds_read_b128 v[182:185], v166 offset:1024
	ds_read_b128 v[186:189], v166 offset:2048
	ds_read_b128 v[190:193], v166 offset:3072
	v_add_u32_e32 v166, 0x1c000, v179
	ds_read_b128 v[194:197], v166
	ds_read_b128 v[198:201], v166 offset:1024
	ds_read_b128 v[202:205], v166 offset:2048
	ds_read_b128 v[206:209], v166 offset:3072
	s_add_i32 s29, s29, 0x80000
	s_mov_b32 m0, s43
	ds_read_b128 v[210:213], v180 offset:32768
	ds_read_b128 v[214:217], v180 offset:33792
	ds_read_b128 v[218:221], v180 offset:34816
	ds_read_b128 v[222:225], v180 offset:35840
	ds_read_b128 v[226:229], v180 offset:36864
	ds_read_b128 v[230:233], v180 offset:37888
	ds_read_b128 v[234:237], v180 offset:38912
	ds_read_b128 v[238:241], v180 offset:39936
	buffer_load_dwordx4 v1, s[4:7], s29 offen lds
	s_mov_b32 m0, s44
	s_nop 0
	buffer_load_dwordx4 v175, s[4:7], s29 offen lds
	s_waitcnt vmcnt(8)
	s_waitcnt lgkmcnt(0)
	s_barrier
	s_waitcnt lgkmcnt(7)
	v_mfma_f32_16x16x32_bf16 v[126:129], v[162:165], v[210:213], v[126:129]
	v_mfma_f32_16x16x32_bf16 v[126:129], v[182:185], v[214:217], v[126:129]
	s_waitcnt lgkmcnt(5)
	v_mfma_f32_16x16x32_bf16 v[122:125], v[190:193], v[214:217], v[122:125]
	v_mfma_f32_16x16x32_bf16 v[122:125], v[186:189], v[210:213], v[122:125]
	s_waitcnt lgkmcnt(3)
	v_mfma_f32_16x16x32_bf16 v[114:117], v[186:189], v[218:221], v[114:117]
	v_mfma_f32_16x16x32_bf16 v[114:117], v[190:193], v[222:225], v[114:117]
	s_waitcnt lgkmcnt(1)
	v_mfma_f32_16x16x32_bf16 v[118:121], v[182:185], v[222:225], v[118:121]
	v_mfma_f32_16x16x32_bf16 v[118:121], v[162:165], v[218:221], v[118:121]
	v_mfma_f32_16x16x32_bf16 v[110:113], v[162:165], v[226:229], v[110:113]
	v_mfma_f32_16x16x32_bf16 v[110:113], v[182:185], v[230:233], v[110:113]
	v_mfma_f32_16x16x32_bf16 v[106:109], v[190:193], v[230:233], v[106:109]
	v_mfma_f32_16x16x32_bf16 v[106:109], v[186:189], v[226:229], v[106:109]
	v_mfma_f32_16x16x32_bf16 v[98:101], v[186:189], v[234:237], v[98:101]
	v_mfma_f32_16x16x32_bf16 v[98:101], v[190:193], v[238:241], v[98:101]
	s_waitcnt lgkmcnt(0)
	v_mfma_f32_16x16x32_bf16 v[102:105], v[182:185], v[238:241], v[102:105]
	v_mfma_f32_16x16x32_bf16 v[102:105], v[162:165], v[234:237], v[102:105]
	v_mfma_f32_16x16x32_bf16 v[94:97], v[194:197], v[210:213], v[94:97]
	v_mfma_f32_16x16x32_bf16 v[94:97], v[198:201], v[214:217], v[94:97]
	v_mfma_f32_16x16x32_bf16 v[90:93], v[206:209], v[214:217], v[90:93]
	v_mfma_f32_16x16x32_bf16 v[90:93], v[202:205], v[210:213], v[90:93]
	v_mfma_f32_16x16x32_bf16 v[82:85], v[202:205], v[218:221], v[82:85]
	v_mfma_f32_16x16x32_bf16 v[82:85], v[206:209], v[222:225], v[82:85]
	v_mfma_f32_16x16x32_bf16 v[86:89], v[198:201], v[222:225], v[86:89]
	v_mfma_f32_16x16x32_bf16 v[86:89], v[194:197], v[218:221], v[86:89]
	v_mfma_f32_16x16x32_bf16 v[78:81], v[194:197], v[226:229], v[78:81]
	v_mfma_f32_16x16x32_bf16 v[78:81], v[198:201], v[230:233], v[78:81]
	v_mfma_f32_16x16x32_bf16 v[74:77], v[206:209], v[230:233], v[74:77]
	v_mfma_f32_16x16x32_bf16 v[74:77], v[202:205], v[226:229], v[74:77]
	v_mfma_f32_16x16x32_bf16 v[66:69], v[202:205], v[234:237], v[66:69]
	v_mfma_f32_16x16x32_bf16 v[66:69], v[206:209], v[238:241], v[66:69]
	v_mfma_f32_16x16x32_bf16 v[70:73], v[198:201], v[238:241], v[70:73]
	v_mfma_f32_16x16x32_bf16 v[70:73], v[194:197], v[234:237], v[70:73]
	s_barrier
	s_mov_b32 m0, s49
	ds_read_b128 v[210:213], v180 offset:49152
	ds_read_b128 v[214:217], v180 offset:50176
	ds_read_b128 v[218:221], v180 offset:51200
	ds_read_b128 v[222:225], v180 offset:52224
	ds_read_b128 v[226:229], v180 offset:53248
	ds_read_b128 v[230:233], v180 offset:54272
	ds_read_b128 v[234:237], v180 offset:55296
	ds_read_b128 v[238:241], v180 offset:56320
	buffer_load_dwordx4 v174, s[8:11], s28 offen lds
	s_mov_b32 m0, s50
	s_add_i32 s27, s27, 0x80080
	buffer_load_dwordx4 v176, s[8:11], s28 offen lds
	s_mov_b32 m0, s53
	s_nop 0
	buffer_load_dwordx4 v174, s[8:11], s27 offen lds
	s_mov_b32 m0, s54
	s_nop 0
	buffer_load_dwordx4 v176, s[8:11], s27 offen lds
	s_mov_b32 m0, s51
	s_nop 0
	buffer_load_dwordx4 v1, s[4:7], s26 offen lds
	s_mov_b32 m0, s52
	s_nop 0
	buffer_load_dwordx4 v175, s[4:7], s26 offen lds
	s_waitcnt vmcnt(8)
	s_waitcnt lgkmcnt(0)
	s_barrier
	s_waitcnt lgkmcnt(7)
	v_mfma_f32_16x16x32_bf16 v[62:65], v[162:165], v[210:213], v[62:65]
	v_mfma_f32_16x16x32_bf16 v[62:65], v[182:185], v[214:217], v[62:65]
	s_waitcnt lgkmcnt(5)
	v_mfma_f32_16x16x32_bf16 v[58:61], v[190:193], v[214:217], v[58:61]
	v_mfma_f32_16x16x32_bf16 v[58:61], v[186:189], v[210:213], v[58:61]
	s_waitcnt lgkmcnt(3)
	v_mfma_f32_16x16x32_bf16 v[50:53], v[186:189], v[218:221], v[50:53]
	v_mfma_f32_16x16x32_bf16 v[50:53], v[190:193], v[222:225], v[50:53]
	s_waitcnt lgkmcnt(1)
	v_mfma_f32_16x16x32_bf16 v[54:57], v[182:185], v[222:225], v[54:57]
	v_mfma_f32_16x16x32_bf16 v[54:57], v[162:165], v[218:221], v[54:57]
	v_mfma_f32_16x16x32_bf16 v[46:49], v[162:165], v[226:229], v[46:49]
	v_mfma_f32_16x16x32_bf16 v[46:49], v[182:185], v[230:233], v[46:49]
	v_mfma_f32_16x16x32_bf16 v[42:45], v[190:193], v[230:233], v[42:45]
	v_mfma_f32_16x16x32_bf16 v[42:45], v[186:189], v[226:229], v[42:45]
	v_mfma_f32_16x16x32_bf16 v[34:37], v[186:189], v[234:237], v[34:37]
	v_mfma_f32_16x16x32_bf16 v[34:37], v[190:193], v[238:241], v[34:37]
	s_waitcnt lgkmcnt(0)
	v_mfma_f32_16x16x32_bf16 v[38:41], v[182:185], v[238:241], v[38:41]
	v_mfma_f32_16x16x32_bf16 v[38:41], v[162:165], v[234:237], v[38:41]
	v_mfma_f32_16x16x32_bf16 v[30:33], v[194:197], v[210:213], v[30:33]
	v_mfma_f32_16x16x32_bf16 v[30:33], v[198:201], v[214:217], v[30:33]
	v_mfma_f32_16x16x32_bf16 v[26:29], v[206:209], v[214:217], v[26:29]
	v_mfma_f32_16x16x32_bf16 v[26:29], v[202:205], v[210:213], v[26:29]
	v_mfma_f32_16x16x32_bf16 v[18:21], v[202:205], v[218:221], v[18:21]
	v_mfma_f32_16x16x32_bf16 v[18:21], v[206:209], v[222:225], v[18:21]
	v_mfma_f32_16x16x32_bf16 v[22:25], v[198:201], v[222:225], v[22:25]
	v_mfma_f32_16x16x32_bf16 v[22:25], v[194:197], v[218:221], v[22:25]
	v_mfma_f32_16x16x32_bf16 v[14:17], v[194:197], v[226:229], v[14:17]
	v_mfma_f32_16x16x32_bf16 v[14:17], v[198:201], v[230:233], v[14:17]
	v_mfma_f32_16x16x32_bf16 v[10:13], v[206:209], v[230:233], v[10:13]
	v_mfma_f32_16x16x32_bf16 v[10:13], v[202:205], v[226:229], v[10:13]
	v_mfma_f32_16x16x32_bf16 v[2:5], v[202:205], v[234:237], v[2:5]
	v_mfma_f32_16x16x32_bf16 v[2:5], v[206:209], v[238:241], v[2:5]
	v_mfma_f32_16x16x32_bf16 v[6:9], v[198:201], v[238:241], v[6:9]
	v_mfma_f32_16x16x32_bf16 v[6:9], v[194:197], v[234:237], v[6:9]
	s_barrier
	s_add_i32 s10, s65, 2
	s_addk_i32 s64, 0x100
	s_cmp_gt_u32 s65, 29
	s_cbranch_scc1 .LBB0_910
	s_mov_b32 s65, s10
	s_branch .LBB0_869
